# diff/swa: next-unit queue atomic issued early (diff: top of last tile; swa: tile-loop exit), unit top only publishes it
# speedup vs baseline: 1.0023x; 1.0023x over previous
; #define LAS __attribute__((address_space(3)))
; __device__ __forceinline__ int lt_tid(int wv) { int ln; asm volatile("v_mbcnt_lo_u32_b32 %0, -1, 0\n\tv_mbcnt_hi_u32_b32 %0, -1, %0" : "=v"(ln)); return (wv << 6) | ln; }
; __device__ __forceinline__ int lt_bid() { int b = blockIdx.x; asm volatile("" : "+s"(b)); return b; }
; __device__ __forceinline__ unsigned char* lt_ptr(unsigned char* q) { unsigned long long a = (unsigned long long)q; asm volatile("" : "+s"(a)); return (unsigned char*)(GAS unsigned char*)a; }
;     const int bid = lt_bid(); unsigned char* const ws = lt_ptr(p.ws); (void)bid;
;     const int tid = lt_tid(wvid), lane = tid & 63, wave = __builtin_amdgcn_readfirstlane(tid >> 6), l31 = lane & 31, hi = lane >> 5;
;     const bf16_t* U = (const bf16_t*)(ws + WS_U); const bf16_t* VT = (const bf16_t*)(ws + WS_VTD); bf16_t* MIX = (bf16_t*)(ws + WS_MIX);
;     unsigned* qhead = (unsigned*)(ws + WS_CTL) + CW_DQ + (qslot * 4 + l) * 64;
;     LAS float* btab = (LAS float*)lds;
;     LAS int* ucur = (LAS int*)(lds + 4 * 132 * 4);
;     LAS unsigned char* KV = lds + 4096;
;     constexpr float LOG2E = 1.4426950408889634f;
;     for (int i = tid; i < 4 * 129; i += NTHR) { const int h = i / 129, n = i % 129; btab[h * 132 + n] = p.in[I_RELB][t5_bucket(n) * 8 + 4 + h] * 5.656854249492381f; }
;     if (tid < 4) { float bx = -1e30f; for (int n = 0; n < 32; ++n) bx = fmaxf(bx, p.in[I_RELB][n * 8 + 4 + tid]); btab[tid * 132 + 129] = bx * 5.656854249492381f; }
;     float s1 = 0.f, s2 = 0.f;
;     for (int i = 0; i < 32; ++i) { s1 += p.in[I_LQ1][l * 32 + i] * p.in[I_LK1][l * 32 + i]; s2 += p.in[I_LQ2][l * 32 + i] * p.in[I_LK2][l * 32 + i]; }
;     const float lam_init = 0.8f - 0.6f * expf(-0.3f * (float)l), lam = expf(s1) - expf(s2) + lam_init;
.LBB0_767:
	s_or_b64 exec, exec, s[0:1]
	s_ashr_i32 s21, s20, 6
	s_add_u32 s8, s6, 0x4090000
	s_addc_u32 s9, s7, 0
	s_add_u32 s42, s6, 0x1e674c00
	v_readlane_b32 s22, v254, 49
	s_addc_u32 s43, s7, 0
	s_lshl_b32 s40, s22, 6
	s_lshl_b64 s[10:11], s[40:41], 2
	s_add_u32 s0, s6, s10
	s_addc_u32 s1, s7, s11
	v_readlane_b32 s48, v253, 12
	s_add_u32 s16, s0, 0x4100
	v_readlane_b32 s56, v253, 20
	v_readlane_b32 s57, v253, 21
	s_addc_u32 s17, s1, 0
	s_lshl_b32 s40, s22, 5
	v_readlane_b32 s58, v253, 22
	v_readlane_b32 s59, v253, 23
	v_readlane_b32 s60, v253, 24
	v_readlane_b32 s61, v253, 25
	v_readlane_b32 s62, v253, 26
	v_readlane_b32 s63, v253, 27
	s_mov_b64 s[24:25], s[56:57]
	s_lshl_b64 s[4:5], s[40:41], 2
	s_mov_b64 s[30:31], s[62:63]
	v_readlane_b32 s49, v253, 13
	v_readlane_b32 s50, v253, 14
	v_readlane_b32 s51, v253, 15
	v_readlane_b32 s52, v253, 16
	v_readlane_b32 s53, v253, 17
	v_readlane_b32 s54, v253, 18
	v_readlane_b32 s55, v253, 19
	s_add_u32 s18, s30, s4
	s_mov_b64 s[26:27], s[58:59]
	s_mov_b64 s[28:29], s[60:61]
	s_addc_u32 s19, s31, s5
	v_readlane_b32 s48, v253, 30
	v_readlane_b32 s49, v253, 31
	s_add_u32 s2, s48, s4
	v_readlane_b32 s50, v253, 32
	s_addc_u32 s3, s49, s5
	v_readlane_b32 s51, v253, 33
	s_add_u32 s0, s50, s4
	v_readlane_b32 s52, v253, 34
	s_addc_u32 s1, s51, s5
	global_load_dwordx4 v[2:5], v1, s[18:19] offset:48
	global_load_dwordx4 v[6:9], v1, s[18:19] offset:32
	global_load_dwordx4 v[10:13], v1, s[18:19] offset:16
	global_load_dwordx4 v[14:17], v1, s[18:19]
	v_readlane_b32 s53, v253, 35
	global_load_dwordx4 v[18:21], v1, s[2:3] offset:48
	global_load_dwordx4 v[22:25], v1, s[2:3] offset:32
	global_load_dwordx4 v[26:29], v1, s[2:3] offset:16
	global_load_dwordx4 v[34:37], v1, s[2:3]
	s_add_u32 s4, s52, s4
	s_addc_u32 s5, s53, s5
	global_load_dwordx4 v[38:41], v1, s[0:1] offset:48
	global_load_dwordx4 v[42:45], v1, s[0:1] offset:32
	global_load_dwordx4 v[46:49], v1, s[0:1] offset:16
	global_load_dwordx4 v[50:53], v1, s[0:1]
	global_load_dwordx4 v[54:57], v1, s[4:5] offset:48
	global_load_dwordx4 v[58:61], v1, s[4:5] offset:32
	global_load_dwordx4 v[62:65], v1, s[4:5] offset:16
	global_load_dwordx4 v[66:69], v1, s[4:5]
	s_lshl_b32 s46, s21, 5
	s_cmp_lt_u32 s20, 64
	v_and_b32_e32 v31, 63, v32
	v_and_b32_e32 v149, 31, v32
	v_bfe_u32 v0, v32, 5, 1
	v_readlane_b32 s54, v253, 36
	v_readlane_b32 s55, v253, 37
	v_lshlrev_b32_e32 v186, 2, v0
	v_mov_b32_e32 v143, v1
	v_mov_b32_e32 v145, v1
	v_mov_b32_e32 v99, v1
	v_mov_b32_e32 v100, v1
	v_mov_b32_e32 v101, v1
	v_readlane_b32 s56, v253, 38
	v_readlane_b32 s57, v253, 39
	v_readlane_b32 s58, v253, 40
	v_readlane_b32 s59, v253, 41
	v_readlane_b32 s60, v253, 42
	v_readlane_b32 s61, v253, 43
	v_readlane_b32 s62, v253, 44
	v_readlane_b32 s63, v253, 45
	s_waitcnt vmcnt(8)
	v_fma_f32 v34, v14, v34, 0
	v_fmac_f32_e32 v34, v15, v35
	v_fmac_f32_e32 v34, v16, v36
	v_fmac_f32_e32 v34, v17, v37
	s_waitcnt vmcnt(0)
	v_fma_f32 v33, v50, v66, 0
	v_fmac_f32_e32 v33, v51, v67
	v_fmac_f32_e32 v33, v52, v68
	v_fmac_f32_e32 v34, v10, v26
	v_fmac_f32_e32 v33, v53, v69
	v_fmac_f32_e32 v34, v11, v27
	v_fmac_f32_e32 v33, v46, v62
	v_fmac_f32_e32 v34, v12, v28
	v_fmac_f32_e32 v33, v47, v63
	v_fmac_f32_e32 v34, v13, v29
	v_fmac_f32_e32 v33, v48, v64
	v_fmac_f32_e32 v34, v6, v22
	v_fmac_f32_e32 v33, v49, v65
	v_fmac_f32_e32 v34, v7, v23
	v_fmac_f32_e32 v33, v42, v58
	v_fmac_f32_e32 v34, v8, v24
	v_fmac_f32_e32 v33, v43, v59
	v_fmac_f32_e32 v34, v9, v25
	v_fmac_f32_e32 v33, v44, v60
	v_fmac_f32_e32 v34, v2, v18
	v_fmac_f32_e32 v33, v45, v61
	v_fmac_f32_e32 v34, v3, v19
	v_fmac_f32_e32 v33, v38, v54
	v_fmac_f32_e32 v34, v4, v20
	v_fmac_f32_e32 v33, v39, v55
	v_fmac_f32_e32 v34, v5, v21
	global_load_dwordx4 v[2:5], v1, s[18:19] offset:112
	global_load_dwordx4 v[10:13], v1, s[18:19] offset:96
	global_load_dwordx4 v[18:21], v1, s[18:19] offset:80
	global_load_dwordx4 v[26:29], v1, s[18:19] offset:64
	global_load_dwordx4 v[6:9], v1, s[2:3] offset:112
	global_load_dwordx4 v[14:17], v1, s[2:3] offset:96
	global_load_dwordx4 v[22:25], v1, s[2:3] offset:80
	global_load_dwordx4 v[36:39], v1, s[2:3] offset:64
	v_fmac_f32_e32 v33, v40, v56
	v_fmac_f32_e32 v33, v41, v57
	global_load_dwordx4 v[40:43], v1, s[0:1] offset:112
	global_load_dwordx4 v[44:47], v1, s[0:1] offset:96
	global_load_dwordx4 v[48:51], v1, s[0:1] offset:80
	global_load_dwordx4 v[52:55], v1, s[0:1] offset:64
	global_load_dwordx4 v[56:59], v1, s[4:5] offset:112
	global_load_dwordx4 v[60:63], v1, s[4:5] offset:96
	global_load_dwordx4 v[64:67], v1, s[4:5] offset:80
	global_load_dwordx4 v[68:71], v1, s[4:5] offset:64
	s_mov_b32 s0, 0x3fb8aa3b
	s_mov_b32 s1, 0xc2ce8ed0
	s_mov_b32 s2, 0x42b17218
	v_readlane_b32 s4, v255, 14
	v_readlane_b32 s5, v255, 15
	s_cselect_b64 s[18:19], -1, 0
	s_lshl_b64 s[26:27], s[4:5], 2
	s_waitcnt vmcnt(8)
;     ...
;     for (int i = 0; i < 32; ++i) { s1 += p.in[I_LQ1][l * 32 + i] * p.in[I_LK1][l * 32 + i]; s2 += p.in[I_LQ2][l * 32 + i] * p.in[I_LK2][l * 32 + i]; }
;     const float lam_init = 0.8f - 0.6f * expf(-0.3f * (float)l), lam = expf(s1) - expf(s2) + lam_init;
;     const float c2 = 0.17677669529663687f * LOG2E;
;     const int krow = tid >> 3, kch = tid & 7;
	v_fmac_f32_e32 v34, v26, v36
	v_fmac_f32_e32 v34, v27, v37
	v_fmac_f32_e32 v34, v28, v38
	v_fmac_f32_e32 v34, v29, v39
	v_fmac_f32_e32 v34, v18, v22
	v_fmac_f32_e32 v34, v19, v23
	v_fmac_f32_e32 v34, v20, v24
	v_fmac_f32_e32 v34, v21, v25
	v_fmac_f32_e32 v34, v10, v14
	v_fmac_f32_e32 v34, v11, v15
	v_fmac_f32_e32 v34, v12, v16
	v_fmac_f32_e32 v34, v13, v17
	v_fmac_f32_e32 v34, v2, v6
	v_cvt_f32_u32_e32 v2, s22
	v_fmac_f32_e32 v34, v3, v7
	v_fmac_f32_e32 v34, v4, v8
	v_fmac_f32_e32 v34, v5, v9
	v_mul_f32_e32 v2, 0xbe99999a, v2
	v_mul_f32_e32 v3, 0x3fb8aa3b, v2
	v_fma_f32 v4, v2, s0, -v3
	v_rndne_f32_e32 v5, v3
	v_fmac_f32_e32 v4, 0x32a5705f, v2
	v_sub_f32_e32 v3, v3, v5
	s_waitcnt vmcnt(0)
	v_fmac_f32_e32 v33, v52, v68
	v_add_f32_e32 v3, v3, v4
	v_fmac_f32_e32 v33, v53, v69
	v_exp_f32_e32 v3, v3
	v_cvt_i32_f32_e32 v4, v5
	v_fmac_f32_e32 v33, v54, v70
	v_fmac_f32_e32 v33, v55, v71
	v_fmac_f32_e32 v33, v48, v64
	v_fmac_f32_e32 v33, v49, v65
	v_ldexp_f32 v3, v3, v4
	v_cmp_ngt_f32_e32 vcc, s1, v2
	v_fmac_f32_e32 v33, v50, v66
	v_mov_b32_e32 v7, 0x7f800000
	v_cndmask_b32_e32 v3, 0, v3, vcc
	v_cmp_nlt_f32_e32 vcc, s2, v2
	v_fmac_f32_e32 v33, v51, v67
	v_fmac_f32_e32 v33, v44, v60
	v_cndmask_b32_e32 v2, v7, v3, vcc
	v_mov_b32_e32 v3, 0x3f4ccccd
	v_fmamk_f32 v3, v2, 0xbf19999a, v3
	v_mul_f32_e32 v2, 0x3fb8aa3b, v34
	v_fmac_f32_e32 v33, v45, v61
	v_fma_f32 v4, v34, s0, -v2
	v_rndne_f32_e32 v5, v2
	v_fmac_f32_e32 v33, v46, v62
	v_fmac_f32_e32 v4, 0x32a5705f, v34
	v_sub_f32_e32 v2, v2, v5
	v_fmac_f32_e32 v33, v47, v63
	v_add_f32_e32 v2, v2, v4
	v_fmac_f32_e32 v33, v40, v56
	v_exp_f32_e32 v2, v2
	v_cvt_i32_f32_e32 v4, v5
	v_fmac_f32_e32 v33, v41, v57
	v_fmac_f32_e32 v33, v42, v58
	v_fmac_f32_e32 v33, v43, v59
	v_ldexp_f32 v2, v2, v4
	v_mul_f32_e32 v4, 0x3fb8aa3b, v33
	v_fma_f32 v5, v33, s0, -v4
	v_rndne_f32_e32 v6, v4
	v_fmac_f32_e32 v5, 0x32a5705f, v33
	v_sub_f32_e32 v4, v4, v6
	v_add_f32_e32 v4, v4, v5
	v_exp_f32_e32 v4, v4
	v_cvt_i32_f32_e32 v5, v6
	v_cmp_ngt_f32_e32 vcc, s1, v34
	v_lshl_add_u32 v6, v31, 4, 0
	s_mul_i32 s0, s21, 0x1800
	v_cndmask_b32_e32 v2, 0, v2, vcc
	v_cmp_nlt_f32_e32 vcc, s2, v34
	v_ldexp_f32 v4, v4, v5
	v_and_b32_e32 v5, 7, v32
	v_cndmask_b32_e32 v2, v7, v2, vcc
	v_cmp_ngt_f32_e32 vcc, s1, v33
	s_add_u32 s1, s6, s26
	s_addc_u32 s4, s7, s27
	v_cndmask_b32_e32 v4, 0, v4, vcc
	v_cmp_nlt_f32_e32 vcc, s2, v33
	s_add_u32 s47, s1, 0x5000
	s_movk_i32 s1, 0xb00
	v_cndmask_b32_e32 v4, v7, v4, vcc
	v_sub_f32_e32 v2, v2, v4
	v_ashrrev_i32_e32 v4, 3, v30
	v_mul_lo_u32 v7, v4, s1
	v_lshlrev_b32_e32 v8, 3, v5
	s_movk_i32 s1, 0x1040
	s_addc_u32 s48, s4, 0
	v_or_b32_e32 v142, v7, v8
	v_mul_lo_u32 v7, v4, s1
	v_mul_lo_u32 v4, v4, s83
	v_lshlrev_b32_e32 v5, 4, v5
	v_add_f32_e32 v184, v3, v2
	v_lshlrev_b32_e32 v2, 3, v0
	v_cmp_gt_u32_e64 s[4:5], 32, v31
	v_add3_u32 v185, 0, v4, v5
	v_lshlrev_b32_e32 v0, 4, v0
	v_mul_u32_u24_e32 v4, 0x90, v149
	v_mov_b32_e32 v5, 0x3f80
	s_add_u32 s20, s54, s10
	v_cmp_eq_u32_e64 s[2:3], 0, v30
	v_or_b32_e32 v144, v7, v8
	v_cndmask_b32_e64 v98, 0, v5, s[4:5]
	v_sub_f32_e32 v187, 1.0, v3
	s_addc_u32 s21, s55, s11
	v_add3_u32 v188, 0, v0, v4
	v_lshlrev_b32_e32 v146, 1, v2
	v_add_u32_e32 v189, s0, v6
	s_and_saveexec_b64 s[0:1], s[2:3]
	s_cbranch_execz .Ldqp0_d
	v_mov_b32_e32 v102, 1
	global_atomic_add v102, v1, v102, s[16:17] sc0
.Ldqp0_d:
	s_or_b64 exec, exec, s[0:1]
	s_branch .LBB0_770

;     ...
;     for (;;) {
;         __syncthreads();
;         if (tid == 0) *ucur = (int)atomicAdd(qhead, 1u);
;         __syncthreads();
;         const int u = *ucur;
.LBB0_770:
	s_waitcnt lgkmcnt(0)
	s_barrier
	s_and_saveexec_b64 s[0:1], s[2:3]
	s_cbranch_execz .LBB0_774
	s_waitcnt vmcnt(0)
	ds_write_b32 v1, v102 offset:2112

;     ...
;         if (tid == 0) *ucur = (int)atomicAdd(qhead, 1u);
;     ...
;         for (int kt = 0; kt < nkt; ++kt) {
;             const int k0 = kt * 64, cur = kt & 1;
;             if (kt + 1 < nkt) { kreg = *(const u32x4*)(kbase + (koff + (unsigned)((k0 + 64) * INW))); vreg = *(const u32x4*)(vbase + (voff + (unsigned)(k0 + 64))); }
.Ldqp_d_in:
	s_and_saveexec_b64 s[0:1], s[2:3]
	s_cbranch_execz .Ldqp_d
	v_mov_b32_e32 v102, 1
	global_atomic_add v102, v1, v102, s[16:17] sc0

; #define LAS __attribute__((address_space(3)))
; __device__ __forceinline__ int lt_tid(int wv) { int ln; asm volatile("v_mbcnt_lo_u32_b32 %0, -1, 0\n\tv_mbcnt_hi_u32_b32 %0, -1, %0" : "=v"(ln)); return (wv << 6) | ln; }
;     ...
;     const int tid = lt_tid(wvid), lane = tid & 63, wave = __builtin_amdgcn_readfirstlane(tid >> 6), l31 = lane & 31, hi = lane >> 5;
;     const bf16_t* U = (const bf16_t*)(ws + WS_U); const bf16_t* VT = (const bf16_t*)(ws + WS_VTA); bf16_t* MIX = (bf16_t*)(ws + WS_MIX);
;     unsigned* qhead = (unsigned*)(ws + WS_CTL) + CW_DQ + (qslot * 4 + 2 + l) * 64;
;     LAS float* btab = (LAS float*)lds;
;     LAS int* ucur = (LAS int*)(lds + 8 * 132 * 4);
;     LAS unsigned char* KV = lds + 8192;
;     constexpr float LOG2E = 1.4426950408889634f;
;     __syncthreads();
;     const float c2 = 0.125f * LOG2E;
;     for (int i = tid; i < 4 * 130; i += NTHR) { const int h = i / 130, n = i % 130;
;         const float bv = n == 0 ? -INFINITY : p.in[I_RELB][t5_bucket(min(n - 1, 128)) * 8 + h] * LOG2E;
;         btab[h * 132 + n] = n == 129 ? -INFINITY : bv; btab[(4 + h) * 132 + n] = bv; }
;     if (tid < 4) { float bx = -1e30f; for (int n = 0; n < 32; ++n) bx = fmaxf(bx, p.in[I_RELB][n * 8 + tid]); btab[tid * 132 + 131] = bx * LOG2E; }
;     const int krow = tid >> 3, kch = tid & 7;
.LBB0_804:
	s_or_b64 exec, exec, s[2:3]
	s_add_u32 s16, s0, 0x4090000
	s_addc_u32 s17, s1, 0
	s_add_u32 s18, s0, 0x1f6b4c00
	s_addc_u32 s19, s1, 0
	s_add_u32 s20, s0, 0xf1f0000
	s_addc_u32 s21, s1, 0
	s_add_u32 s2, s0, s10
	s_addc_u32 s3, s1, s11
	s_add_u32 s22, s2, 0x4300
	s_addc_u32 s23, s3, 0
	s_bfe_u32 s4, s24, 0x20006
	s_ashr_i32 s34, s24, 8
	s_lshl_b32 s35, s4, 5
	s_cmp_eq_u32 s4, 0
	s_cselect_b64 s[24:25], -1, 0
	s_add_u32 s0, s0, s26
	s_addc_u32 s1, s1, s27
	s_add_u32 s26, s0, 0x5200
	v_readlane_b32 s0, v254, 49
	v_ashrrev_i32_e32 v4, 3, v2
	v_and_b32_e32 v5, 7, v6
	s_addc_u32 s27, s1, 0
	s_lshl_b32 s36, s0, 2
	s_movk_i32 s0, 0xb00
	v_and_b32_e32 v112, 31, v6
	v_bfe_u32 v3, v6, 5, 1
	v_cmp_eq_u32_e64 s[2:3], 0, v2
	v_mul_lo_u32 v2, v4, s0
	v_lshlrev_b32_e32 v6, 3, v5
	s_movk_i32 s0, 0x1040
	v_or_b32_e32 v98, v2, v6
	v_mul_lo_u32 v2, v4, s0
	v_or_b32_e32 v100, v2, v6
	v_mul_lo_u32 v2, v4, s83
	v_lshlrev_b32_e32 v4, 4, v5
	v_add3_u32 v113, 0, v2, v4
	v_cmp_eq_u32_e64 s[4:5], 0, v3
	v_mov_b32_e32 v2, 0x3f80
	v_mul_u32_u24_e32 v4, 0x90, v112
	v_cndmask_b32_e64 v66, 0, v2, s[4:5]
	v_lshlrev_b32_e32 v2, 4, v3
	s_sub_i32 s0, s35, 59
	v_lshlrev_b32_e32 v0, 3, v3
	v_lshlrev_b32_e32 v114, 2, v3
	v_add3_u32 v115, 0, v2, v4
	v_add_u32_e32 v2, s0, v112
	v_mov_b32_e32 v99, v1
	v_mov_b32_e32 v101, v1
	v_mov_b32_e32 v67, v1
	v_mov_b32_e32 v68, v1
	v_mov_b32_e32 v69, v1
	v_not_b32_e32 v116, v114
	v_add_u32_e32 v117, 0x2c000, v98
	v_add_u32_e32 v118, 64, v100
	v_sub_u32_e32 v119, v2, v114
	s_waitcnt vmcnt(1)
	v_lshlrev_b32_e32 v102, 1, v0
	s_and_saveexec_b64 s[0:1], s[2:3]
	s_cbranch_execz .Ldqp0_s
	v_mov_b32_e32 v223, 1
	global_atomic_add v223, v1, v223, s[22:23] sc0

;     ...
;     for (;;) {
;         __syncthreads();
;         if (tid == 0) *ucur = (int)atomicAdd(qhead, 1u);
;         __syncthreads();
;         const int u = *ucur;
.LBB0_807:
	s_waitcnt lgkmcnt(0)
	s_barrier
	s_and_saveexec_b64 s[0:1], s[2:3]
	s_cbranch_execz .LBB0_811
	s_waitcnt vmcnt(0)
	ds_write_b32 v1, v223 offset:4224

; __device__ __forceinline__ int lt_tid(int wv) { int ln; asm volatile("v_mbcnt_lo_u32_b32 %0, -1, 0\n\tv_mbcnt_hi_u32_b32 %0, -1, %0" : "=v"(ln)); return (wv << 6) | ln; }
; __device__ __forceinline__ unsigned pkbf(float lo, float hi) { f32x2_t v = {lo, hi}; bf16x2_t b = __builtin_convertvector(v, bf16x2_t); return __builtin_bit_cast(unsigned, b); }
;     ...
;         const float lt = lsum + __shfl_xor(lsum, 32), inv = 1.0f / lt;
;         const int lane2 = lt_tid(wvid) & 63, qpos2 = q0w + (lane2 & 31), hi2 = lane2 >> 5;
;         if (wave_on && qpos2 < LT && (qi > 0 || qpos2 < NMETA)) {
;             bf16_t* orow = MIX + ((size_t)b * LT + qpos2) * D + M_A + hq * 64;
; #pragma unroll
;             for (int d = 0; d < 2; ++d)
; #pragma unroll
;                 for (int g4 = 0; g4 < 4; ++g4) { const int dv0 = 32 * d + 8 * g4 + 4 * hi2;
;                     u32x2 w; w.x = pkbf(O[d][4 * g4] * inv, O[d][4 * g4 + 1] * inv); w.y = pkbf(O[d][4 * g4 + 2] * inv, O[d][4 * g4 + 3] * inv);
;                     *(u32x2*)(orow + dv0) = w; }
.LBB0_833:
	s_and_saveexec_b64 s[0:1], s[2:3]
	s_cbranch_execz .Ldqp_s
	v_mov_b32_e32 v223, 1
	global_atomic_add v223, v1, v223, s[22:23] sc0
.Ldqp_s:
	s_or_b64 exec, exec, s[0:1]
	ds_bpermute_b32 v35, v103, v121
	v_mbcnt_lo_u32_b32 v34, -1, 0
	v_mbcnt_hi_u32_b32 v34, -1, v34
	s_and_b64 s[0:1], s[6:7], exec
	v_and_b32_e32 v0, 31, v34
	v_add_u32_e32 v0, v0, v120
	s_cselect_b32 s0, 0x1010, 16
	v_cmp_gt_i32_e32 vcc, s0, v0
	s_and_b64 s[0:1], s[28:29], vcc
	s_and_saveexec_b64 s[6:7], s[0:1]
	s_xor_b64 s[0:1], exec, s[6:7]
	s_cbranch_execz .LBB0_805
	s_waitcnt lgkmcnt(0)
	v_add_f32_e32 v35, v121, v35
	v_div_scale_f32 v36, s[6:7], v35, v35, 1.0
	v_rcp_f32_e32 v37, v36
	v_div_scale_f32 v38, vcc, 1.0, v35, 1.0
	v_fma_f32 v39, -v36, v37, 1.0
	v_fmac_f32_e32 v37, v39, v37
	v_mul_f32_e32 v39, v38, v37
	v_fma_f32 v40, -v36, v39, v38
	v_fmac_f32_e32 v39, v40, v37
	v_fma_f32 v36, -v36, v39, v38
	v_div_fmas_f32 v36, v36, v37, v39
	v_lshl_add_u64 v[38:39], v[0:1], 0, v[104:105]
	v_lshlrev_b64 v[38:39], 11, v[38:39]
	v_div_fixup_f32 v36, v36, v35, 1.0
	v_lshl_add_u64 v[38:39], s[20:21], 0, v[38:39]
	v_lshrrev_b32_e32 v0, 2, v34
	v_lshl_add_u64 v[38:39], v[106:107], 1, v[38:39]
	v_pk_mul_f32 v[18:19], v[18:19], v[36:37] op_sel_hi:[1,0]
	v_pk_mul_f32 v[20:21], v[20:21], v[36:37] op_sel_hi:[1,0]
	v_and_b32_e32 v0, 8, v0
	v_pk_mul_f32 v[2:3], v[2:3], v[36:37] op_sel_hi:[1,0]
	v_pk_mul_f32 v[4:5], v[4:5], v[36:37] op_sel_hi:[1,0]
	v_cvt_pk_bf16_f32 v18, v18, v19
	v_cvt_pk_bf16_f32 v19, v20, v21
	v_lshl_add_u64 v[20:21], v[38:39], 0, v[0:1]
	v_cvt_pk_bf16_f32 v2, v2, v3
	v_cvt_pk_bf16_f32 v3, v4, v5
	global_store_dwordx2 v[20:21], v[18:19], off
	v_pk_mul_f32 v[18:19], v[22:23], v[36:37] op_sel_hi:[1,0]
	v_pk_mul_f32 v[22:23], v[24:25], v[36:37] op_sel_hi:[1,0]
	global_store_dwordx2 v[20:21], v[2:3], off offset:64
	v_pk_mul_f32 v[2:3], v[6:7], v[36:37] op_sel_hi:[1,0]
	v_pk_mul_f32 v[4:5], v[8:9], v[36:37] op_sel_hi:[1,0]
	v_cvt_pk_bf16_f32 v18, v18, v19
	v_cvt_pk_bf16_f32 v19, v22, v23
	v_cvt_pk_bf16_f32 v2, v2, v3
	v_cvt_pk_bf16_f32 v3, v4, v5
	global_store_dwordx2 v[20:21], v[18:19], off offset:16
	v_pk_mul_f32 v[18:19], v[26:27], v[36:37] op_sel_hi:[1,0]
	v_pk_mul_f32 v[22:23], v[28:29], v[36:37] op_sel_hi:[1,0]
	global_store_dwordx2 v[20:21], v[2:3], off offset:80
	v_pk_mul_f32 v[2:3], v[10:11], v[36:37] op_sel_hi:[1,0]
	v_pk_mul_f32 v[4:5], v[12:13], v[36:37] op_sel_hi:[1,0]
	v_cvt_pk_bf16_f32 v18, v18, v19
	v_cvt_pk_bf16_f32 v19, v22, v23
	v_cvt_pk_bf16_f32 v2, v2, v3
	v_cvt_pk_bf16_f32 v3, v4, v5
	global_store_dwordx2 v[20:21], v[18:19], off offset:32
	v_pk_mul_f32 v[18:19], v[30:31], v[36:37] op_sel_hi:[1,0]
	v_pk_mul_f32 v[22:23], v[32:33], v[36:37] op_sel_hi:[1,0]
	global_store_dwordx2 v[20:21], v[2:3], off offset:96
	v_pk_mul_f32 v[2:3], v[14:15], v[36:37] op_sel_hi:[1,0]
	v_pk_mul_f32 v[4:5], v[16:17], v[36:37] op_sel_hi:[1,0]
	v_cvt_pk_bf16_f32 v18, v18, v19
	v_cvt_pk_bf16_f32 v19, v22, v23
	v_cvt_pk_bf16_f32 v2, v2, v3
	v_cvt_pk_bf16_f32 v3, v4, v5
	global_store_dwordx2 v[20:21], v[18:19], off offset:48
	global_store_dwordx2 v[20:21], v[2:3], off offset:112
	s_branch .LBB0_805
